# t22
# speedup vs baseline: 1.0497x; 1.0078x over previous
_Z11align_fusedPKfS0_PKiPf:
	s_load_dwordx8 s[4:11], s[0:1], 0x0
	s_sub_u32 s2, 0x1fff, s2
	s_mul_i32 s12, s2, 0x5dc0
	v_and_b32_e32 v7, 63, v0
	v_readfirstlane_b32 s13, v0
	v_lshlrev_b32_e32 v1, 4, v7
	v_mul_u32_u24_e32 v3, 12, v7
	s_mul_i32 s18, s13, 96
	s_mul_i32 s3, s13, 6
	s_sub_u32 s3, 0x49c, s3
	v_cmp_gt_u32_e64 s[14:15], s3, v7
	v_add_u32_e32 v2, s18, v1
	v_add_u32_e32 v3, s18, v3
	v_add_u32_e32 v4, 0x600, v3
	s_add_u32 s12, s12, s18
	s_add_u32 s12, s12, 0x800
	s_waitcnt lgkmcnt(0)
	s_sub_u32 s44, s12, 0x800
	s_add_u32 s40, s4, s44
	s_addc_u32 s41, s5, 0
	s_add_u32 s42, s40, 0x1000
	s_addc_u32 s43, s41, 0
	s_add_u32 s4, s4, s12
	s_addc_u32 s5, s5, 0
	s_add_u32 s10, s10, s12
	s_addc_u32 s11, s11, 0
	s_cmp_lg_u32 s13, 0
	s_cbranch_scc1 .Lbulk_waves
	v_lshlrev_b32_e32 v5, 2, v7
	global_load_dword v5, v5, s[8:9]
	global_load_dwordx3 v[44:46], v3, s[6:7]
	s_mov_b32 m0, s18
	s_nop 0
	global_load_lds_dwordx4 v1, s[40:41] nt
	global_load_lds_dwordx4 v1, s[40:41] offset:1024 nt
	global_load_lds_dwordx4 v1, s[40:41] offset:2048 nt
	global_load_lds_dwordx4 v1, s[40:41] offset:3072 nt
	s_add_u32 m0, s18, 0x1000
	s_nop 0
	global_load_lds_dwordx4 v1, s[42:43] nt
	global_load_lds_dwordx4 v1, s[42:43] offset:1024 nt
	s_mov_b32 s20, 0
	s_mov_b32 s21, 0x10000
	s_mov_b32 s22, 0
	s_mov_b32 s23, 0x20000
	s_mov_b32 s24, 0
	s_mov_b32 s25, 0x40000
	s_mov_b32 s26, 0
	s_mov_b32 s27, 0x80000
	s_waitcnt vmcnt(6)
	v_mul_u32_u24_e32 v5, 12, v5
	v_add_f32_dpp v52, v44, v44 quad_perm:[1,0,3,2] row_mask:0xf bank_mask:0xf
	v_add_f32_dpp v53, v45, v45 quad_perm:[1,0,3,2] row_mask:0xf bank_mask:0xf
	v_add_f32_dpp v54, v46, v46 quad_perm:[1,0,3,2] row_mask:0xf bank_mask:0xf
	v_add_f32_dpp v52, v52, v52 quad_perm:[2,3,0,1] row_mask:0xf bank_mask:0xf
	v_add_f32_dpp v53, v53, v53 quad_perm:[2,3,0,1] row_mask:0xf bank_mask:0xf
	v_add_f32_dpp v54, v54, v54 quad_perm:[2,3,0,1] row_mask:0xf bank_mask:0xf
	v_add_f32_dpp v52, v52, v52 row_half_mirror row_mask:0xf bank_mask:0xf
	v_add_f32_dpp v53, v53, v53 row_half_mirror row_mask:0xf bank_mask:0xf
	v_add_f32_dpp v54, v54, v54 row_half_mirror row_mask:0xf bank_mask:0xf
	v_add_f32_dpp v52, v52, v52 row_mirror row_mask:0xf bank_mask:0xf
	v_add_f32_dpp v53, v53, v53 row_mirror row_mask:0xf bank_mask:0xf
	v_add_f32_dpp v54, v54, v54 row_mirror row_mask:0xf bank_mask:0xf
	v_add_f32_dpp v52, v52, v52 row_bcast:15 row_mask:0xa bank_mask:0xf
	v_add_f32_dpp v53, v53, v53 row_bcast:15 row_mask:0xa bank_mask:0xf
	v_add_f32_dpp v54, v54, v54 row_bcast:15 row_mask:0xa bank_mask:0xf
	v_add_f32_dpp v52, v52, v52 row_bcast:31 row_mask:0xc bank_mask:0xf
	v_add_f32_dpp v53, v53, v53 row_bcast:31 row_mask:0xc bank_mask:0xf
	v_add_f32_dpp v54, v54, v54 row_bcast:31 row_mask:0xc bank_mask:0xf
	v_readlane_b32 s28, v52, 63
	v_readlane_b32 s29, v53, 63
	v_readlane_b32 s30, v54, 63
	v_mov_b32_e32 v52, s28
	v_mov_b32_e32 v53, s29
	v_mov_b32_e32 v54, s30
	v_fmac_f32_e32 v44, 0xbc800000, v52
	v_fmac_f32_e32 v45, 0xbc800000, v53
	v_fmac_f32_e32 v46, 0xbc800000, v54
	s_waitcnt vmcnt(0)
	s_waitcnt lgkmcnt(0)
	s_barrier
	ds_read_b32 v48, v5
	ds_read_b32 v49, v5 offset:4
	ds_read_b32 v50, v5 offset:8
	s_waitcnt lgkmcnt(0)
	v_add_f32_dpp v52, v48, v48 quad_perm:[1,0,3,2] row_mask:0xf bank_mask:0xf
	v_add_f32_dpp v53, v49, v49 quad_perm:[1,0,3,2] row_mask:0xf bank_mask:0xf
	v_add_f32_dpp v54, v50, v50 quad_perm:[1,0,3,2] row_mask:0xf bank_mask:0xf
	v_add_f32_dpp v52, v52, v52 quad_perm:[2,3,0,1] row_mask:0xf bank_mask:0xf
	v_add_f32_dpp v53, v53, v53 quad_perm:[2,3,0,1] row_mask:0xf bank_mask:0xf
	v_add_f32_dpp v54, v54, v54 quad_perm:[2,3,0,1] row_mask:0xf bank_mask:0xf
	v_add_f32_dpp v52, v52, v52 row_half_mirror row_mask:0xf bank_mask:0xf
	v_add_f32_dpp v53, v53, v53 row_half_mirror row_mask:0xf bank_mask:0xf
	v_add_f32_dpp v54, v54, v54 row_half_mirror row_mask:0xf bank_mask:0xf
	v_add_f32_dpp v52, v52, v52 row_mirror row_mask:0xf bank_mask:0xf
	v_add_f32_dpp v53, v53, v53 row_mirror row_mask:0xf bank_mask:0xf
	v_add_f32_dpp v54, v54, v54 row_mirror row_mask:0xf bank_mask:0xf
	v_add_f32_dpp v52, v52, v52 row_bcast:15 row_mask:0xa bank_mask:0xf
	v_add_f32_dpp v53, v53, v53 row_bcast:15 row_mask:0xa bank_mask:0xf
	v_add_f32_dpp v54, v54, v54 row_bcast:15 row_mask:0xa bank_mask:0xf
	v_add_f32_dpp v52, v52, v52 row_bcast:31 row_mask:0xc bank_mask:0xf
	v_add_f32_dpp v53, v53, v53 row_bcast:31 row_mask:0xc bank_mask:0xf
	v_add_f32_dpp v54, v54, v54 row_bcast:31 row_mask:0xc bank_mask:0xf
	v_readlane_b32 s32, v52, 63
	v_readlane_b32 s33, v53, 63
	v_readlane_b32 s34, v54, 63
	v_mov_b32_e32 v52, s32
	v_mov_b32_e32 v53, s33
	v_mov_b32_e32 v54, s34
	v_fmac_f32_e32 v48, 0xbc800000, v52
	v_fmac_f32_e32 v49, 0xbc800000, v53
	v_fmac_f32_e32 v50, 0xbc800000, v54
	v_mul_f32_e32 v52, v48, v44
	v_mul_f32_e32 v53, v48, v45
	v_mul_f32_e32 v54, v48, v46
	v_mul_f32_e32 v55, v49, v44
	v_mul_f32_e32 v56, v49, v45
	v_mul_f32_e32 v57, v49, v46
	v_mul_f32_e32 v58, v50, v44
	v_mul_f32_e32 v59, v50, v45
	v_mul_f32_e32 v60, v50, v46
	v_add_f32_dpp v52, v52, v52 quad_perm:[1,0,3,2] row_mask:0xf bank_mask:0xf
	v_add_f32_dpp v53, v53, v53 quad_perm:[1,0,3,2] row_mask:0xf bank_mask:0xf
	v_add_f32_dpp v54, v54, v54 quad_perm:[1,0,3,2] row_mask:0xf bank_mask:0xf
	v_add_f32_dpp v55, v55, v55 quad_perm:[1,0,3,2] row_mask:0xf bank_mask:0xf
	v_add_f32_dpp v56, v56, v56 quad_perm:[1,0,3,2] row_mask:0xf bank_mask:0xf
	v_add_f32_dpp v57, v57, v57 quad_perm:[1,0,3,2] row_mask:0xf bank_mask:0xf
	v_add_f32_dpp v58, v58, v58 quad_perm:[1,0,3,2] row_mask:0xf bank_mask:0xf
	v_add_f32_dpp v59, v59, v59 quad_perm:[1,0,3,2] row_mask:0xf bank_mask:0xf
	v_add_f32_dpp v60, v60, v60 quad_perm:[1,0,3,2] row_mask:0xf bank_mask:0xf
	v_add_f32_dpp v52, v52, v52 quad_perm:[2,3,0,1] row_mask:0xf bank_mask:0xf
	v_add_f32_dpp v53, v53, v53 quad_perm:[2,3,0,1] row_mask:0xf bank_mask:0xf
	v_add_f32_dpp v54, v54, v54 quad_perm:[2,3,0,1] row_mask:0xf bank_mask:0xf
	v_add_f32_dpp v55, v55, v55 quad_perm:[2,3,0,1] row_mask:0xf bank_mask:0xf
	v_add_f32_dpp v56, v56, v56 quad_perm:[2,3,0,1] row_mask:0xf bank_mask:0xf
	v_add_f32_dpp v57, v57, v57 quad_perm:[2,3,0,1] row_mask:0xf bank_mask:0xf
	v_add_f32_dpp v58, v58, v58 quad_perm:[2,3,0,1] row_mask:0xf bank_mask:0xf
	v_add_f32_dpp v59, v59, v59 quad_perm:[2,3,0,1] row_mask:0xf bank_mask:0xf
	v_add_f32_dpp v60, v60, v60 quad_perm:[2,3,0,1] row_mask:0xf bank_mask:0xf
	v_add_f32_dpp v52, v52, v52 row_half_mirror row_mask:0xf bank_mask:0xf
	v_add_f32_dpp v53, v53, v53 row_half_mirror row_mask:0xf bank_mask:0xf
	v_add_f32_dpp v54, v54, v54 row_half_mirror row_mask:0xf bank_mask:0xf
	v_add_f32_dpp v55, v55, v55 row_half_mirror row_mask:0xf bank_mask:0xf
	v_add_f32_dpp v56, v56, v56 row_half_mirror row_mask:0xf bank_mask:0xf
	v_add_f32_dpp v57, v57, v57 row_half_mirror row_mask:0xf bank_mask:0xf
	v_add_f32_dpp v58, v58, v58 row_half_mirror row_mask:0xf bank_mask:0xf
	v_add_f32_dpp v59, v59, v59 row_half_mirror row_mask:0xf bank_mask:0xf
	v_add_f32_dpp v60, v60, v60 row_half_mirror row_mask:0xf bank_mask:0xf
	v_add_f32_dpp v52, v52, v52 row_mirror row_mask:0xf bank_mask:0xf
	v_add_f32_dpp v53, v53, v53 row_mirror row_mask:0xf bank_mask:0xf
	v_add_f32_dpp v54, v54, v54 row_mirror row_mask:0xf bank_mask:0xf
	v_add_f32_dpp v55, v55, v55 row_mirror row_mask:0xf bank_mask:0xf
	v_add_f32_dpp v56, v56, v56 row_mirror row_mask:0xf bank_mask:0xf
	v_add_f32_dpp v57, v57, v57 row_mirror row_mask:0xf bank_mask:0xf
	v_add_f32_dpp v58, v58, v58 row_mirror row_mask:0xf bank_mask:0xf
	v_add_f32_dpp v59, v59, v59 row_mirror row_mask:0xf bank_mask:0xf
	v_add_f32_dpp v60, v60, v60 row_mirror row_mask:0xf bank_mask:0xf
	v_add_f32_dpp v52, v52, v52 row_bcast:15 row_mask:0xa bank_mask:0xf
	v_add_f32_dpp v53, v53, v53 row_bcast:15 row_mask:0xa bank_mask:0xf
	v_add_f32_dpp v54, v54, v54 row_bcast:15 row_mask:0xa bank_mask:0xf
	v_add_f32_dpp v55, v55, v55 row_bcast:15 row_mask:0xa bank_mask:0xf
	v_add_f32_dpp v56, v56, v56 row_bcast:15 row_mask:0xa bank_mask:0xf
	v_add_f32_dpp v57, v57, v57 row_bcast:15 row_mask:0xa bank_mask:0xf
	v_add_f32_dpp v58, v58, v58 row_bcast:15 row_mask:0xa bank_mask:0xf
	v_add_f32_dpp v59, v59, v59 row_bcast:15 row_mask:0xa bank_mask:0xf
	v_add_f32_dpp v60, v60, v60 row_bcast:15 row_mask:0xa bank_mask:0xf
	v_add_f32_dpp v52, v52, v52 row_bcast:31 row_mask:0xc bank_mask:0xf
	v_add_f32_dpp v53, v53, v53 row_bcast:31 row_mask:0xc bank_mask:0xf
	v_add_f32_dpp v54, v54, v54 row_bcast:31 row_mask:0xc bank_mask:0xf
	v_add_f32_dpp v55, v55, v55 row_bcast:31 row_mask:0xc bank_mask:0xf
	v_add_f32_dpp v56, v56, v56 row_bcast:31 row_mask:0xc bank_mask:0xf
	v_add_f32_dpp v57, v57, v57 row_bcast:31 row_mask:0xc bank_mask:0xf
	v_add_f32_dpp v58, v58, v58 row_bcast:31 row_mask:0xc bank_mask:0xf
	v_add_f32_dpp v59, v59, v59 row_bcast:31 row_mask:0xc bank_mask:0xf
	v_add_f32_dpp v60, v60, v60 row_bcast:31 row_mask:0xc bank_mask:0xf
	v_cndmask_b32_e64 v52, v52, v55, s[22:23]
	v_cndmask_b32_e64 v53, v53, v56, s[22:23]
	v_cndmask_b32_e64 v54, v54, v57, s[22:23]
	v_cndmask_b32_e64 v52, v52, v58, s[24:25]
	v_cndmask_b32_e64 v53, v53, v59, s[24:25]
	v_cndmask_b32_e64 v54, v54, v60, s[24:25]
	v_cndmask_b32_e64 v52, v52, 0, s[26:27]
	v_cndmask_b32_e64 v53, v53, 0, s[26:27]
	v_cndmask_b32_e64 v54, v54, 0, s[26:27]
	v_cndmask_b32_e64 v40, 0, 1.0, s[20:21]
	v_cndmask_b32_e64 v41, 0, 1.0, s[22:23]
	v_cndmask_b32_e64 v42, 0, 1.0, s[24:25]
	v_mul_f32_e32 v55, v52, v52
	v_mul_f32_e32 v56, v53, v53
	v_mul_f32_e32 v57, v52, v53
	v_add_f32_dpp v55, v55, v55 quad_perm:[1,0,3,2] row_mask:0xf bank_mask:0xf
	v_add_f32_dpp v56, v56, v56 quad_perm:[1,0,3,2] row_mask:0xf bank_mask:0xf
	v_add_f32_dpp v57, v57, v57 quad_perm:[1,0,3,2] row_mask:0xf bank_mask:0xf
	v_add_f32_dpp v55, v55, v55 quad_perm:[2,3,0,1] row_mask:0xf bank_mask:0xf
	v_add_f32_dpp v56, v56, v56 quad_perm:[2,3,0,1] row_mask:0xf bank_mask:0xf
	v_add_f32_dpp v57, v57, v57 quad_perm:[2,3,0,1] row_mask:0xf bank_mask:0xf
	v_sub_f32_e32 v60, v56, v55
	v_mul_f32_e32 v58, v57, v57
	v_cmp_gt_f32_e32 vcc, 0, v60
	v_mul_f32_e32 v59, v60, v60
	v_fmac_f32_e32 v59, 4.0, v58
	v_sqrt_f32_e32 v59, v59
	s_nop 0
	v_add_f32_e64 v59, |v60|, v59
	v_add_f32_e32 v59, 0x0da24260, v59
	v_rcp_f32_e32 v59, v59
	v_add_f32_e32 v58, v57, v57
	v_mul_f32_e32 v59, v58, v59
	v_cndmask_b32_e64 v59, v59, -v59, vcc
	v_fma_f32 v58, v59, v59, 1.0
	v_rsq_f32_e32 v61, v58
	s_nop 0
	v_mul_f32_e32 v62, v61, v59
	v_mul_f32_e32 v55, v62, v53
	v_mul_f32_e32 v56, v62, v52
	v_fma_f32 v52, v61, v52, -v55
	v_fma_f32 v53, v61, v53, v56
	v_mul_f32_e32 v55, v52, v52
	v_mul_f32_e32 v56, v54, v54
	v_mul_f32_e32 v57, v52, v54
	v_add_f32_dpp v55, v55, v55 quad_perm:[1,0,3,2] row_mask:0xf bank_mask:0xf
	v_add_f32_dpp v56, v56, v56 quad_perm:[1,0,3,2] row_mask:0xf bank_mask:0xf
	v_add_f32_dpp v57, v57, v57 quad_perm:[1,0,3,2] row_mask:0xf bank_mask:0xf
	v_add_f32_dpp v55, v55, v55 quad_perm:[2,3,0,1] row_mask:0xf bank_mask:0xf
	v_add_f32_dpp v56, v56, v56 quad_perm:[2,3,0,1] row_mask:0xf bank_mask:0xf
	v_add_f32_dpp v57, v57, v57 quad_perm:[2,3,0,1] row_mask:0xf bank_mask:0xf
	v_sub_f32_e32 v60, v56, v55
	v_mul_f32_e32 v58, v57, v57
	v_cmp_gt_f32_e32 vcc, 0, v60
	v_mul_f32_e32 v59, v60, v60
	v_fmac_f32_e32 v59, 4.0, v58
	v_sqrt_f32_e32 v59, v59
	v_mul_f32_e32 v63, v62, v41
	v_mul_f32_e32 v43, v62, v40
	v_fma_f32 v40, v61, v40, -v63
	v_fma_f32 v41, v61, v41, v43
	v_add_f32_e64 v59, |v60|, v59
	v_add_f32_e32 v59, 0x0da24260, v59
	v_rcp_f32_e32 v59, v59
	v_add_f32_e32 v58, v57, v57
	v_mul_f32_e32 v59, v58, v59
	v_cndmask_b32_e64 v59, v59, -v59, vcc
	v_fma_f32 v58, v59, v59, 1.0
	v_rsq_f32_e32 v61, v58
	s_nop 0
	v_mul_f32_e32 v62, v61, v59
	v_mul_f32_e32 v55, v62, v54
	v_mul_f32_e32 v56, v62, v52
	v_fma_f32 v52, v61, v52, -v55
	v_fma_f32 v54, v61, v54, v56
	v_mul_f32_e32 v55, v53, v53
	v_mul_f32_e32 v56, v54, v54
	v_mul_f32_e32 v57, v53, v54
	v_add_f32_dpp v55, v55, v55 quad_perm:[1,0,3,2] row_mask:0xf bank_mask:0xf
	v_add_f32_dpp v56, v56, v56 quad_perm:[1,0,3,2] row_mask:0xf bank_mask:0xf
	v_add_f32_dpp v57, v57, v57 quad_perm:[1,0,3,2] row_mask:0xf bank_mask:0xf
	v_add_f32_dpp v55, v55, v55 quad_perm:[2,3,0,1] row_mask:0xf bank_mask:0xf
	v_add_f32_dpp v56, v56, v56 quad_perm:[2,3,0,1] row_mask:0xf bank_mask:0xf
	v_add_f32_dpp v57, v57, v57 quad_perm:[2,3,0,1] row_mask:0xf bank_mask:0xf
	v_sub_f32_e32 v60, v56, v55
	v_mul_f32_e32 v58, v57, v57
	v_cmp_gt_f32_e32 vcc, 0, v60
	v_mul_f32_e32 v59, v60, v60
	v_fmac_f32_e32 v59, 4.0, v58
	v_sqrt_f32_e32 v59, v59
	v_mul_f32_e32 v63, v62, v42
	v_mul_f32_e32 v43, v62, v40
	v_fma_f32 v40, v61, v40, -v63
	v_fma_f32 v42, v61, v42, v43
	v_add_f32_e64 v59, |v60|, v59
	v_add_f32_e32 v59, 0x0da24260, v59
	v_rcp_f32_e32 v59, v59
	v_add_f32_e32 v58, v57, v57
	v_mul_f32_e32 v59, v58, v59
	v_cndmask_b32_e64 v59, v59, -v59, vcc
	v_fma_f32 v58, v59, v59, 1.0
	v_rsq_f32_e32 v61, v58
	s_nop 0
	v_mul_f32_e32 v62, v61, v59
	v_mul_f32_e32 v55, v62, v54
	v_mul_f32_e32 v56, v62, v53
	v_fma_f32 v53, v61, v53, -v55
	v_fma_f32 v54, v61, v54, v56
	v_mul_f32_e32 v55, v52, v52
	v_mul_f32_e32 v56, v53, v53
	v_mul_f32_e32 v57, v52, v53
	v_add_f32_dpp v55, v55, v55 quad_perm:[1,0,3,2] row_mask:0xf bank_mask:0xf
	v_add_f32_dpp v56, v56, v56 quad_perm:[1,0,3,2] row_mask:0xf bank_mask:0xf
	v_add_f32_dpp v57, v57, v57 quad_perm:[1,0,3,2] row_mask:0xf bank_mask:0xf
	v_add_f32_dpp v55, v55, v55 quad_perm:[2,3,0,1] row_mask:0xf bank_mask:0xf
	v_add_f32_dpp v56, v56, v56 quad_perm:[2,3,0,1] row_mask:0xf bank_mask:0xf
	v_add_f32_dpp v57, v57, v57 quad_perm:[2,3,0,1] row_mask:0xf bank_mask:0xf
	v_sub_f32_e32 v60, v56, v55
	v_mul_f32_e32 v58, v57, v57
	v_cmp_gt_f32_e32 vcc, 0, v60
	v_mul_f32_e32 v59, v60, v60
	v_fmac_f32_e32 v59, 4.0, v58
	v_sqrt_f32_e32 v59, v59
	v_mul_f32_e32 v63, v62, v42
	v_mul_f32_e32 v43, v62, v41
	v_fma_f32 v41, v61, v41, -v63
	v_fma_f32 v42, v61, v42, v43
	v_add_f32_e64 v59, |v60|, v59
	v_add_f32_e32 v59, 0x0da24260, v59
	v_rcp_f32_e32 v59, v59
	v_add_f32_e32 v58, v57, v57
	v_mul_f32_e32 v59, v58, v59
	v_cndmask_b32_e64 v59, v59, -v59, vcc
	v_fma_f32 v58, v59, v59, 1.0
	v_rsq_f32_e32 v61, v58
	s_nop 0
	v_mul_f32_e32 v62, v61, v59
	v_mul_f32_e32 v55, v62, v53
	v_mul_f32_e32 v56, v62, v52
	v_fma_f32 v52, v61, v52, -v55
	v_fma_f32 v53, v61, v53, v56
	v_mul_f32_e32 v55, v52, v52
	v_mul_f32_e32 v56, v54, v54
	v_mul_f32_e32 v57, v52, v54
	v_add_f32_dpp v55, v55, v55 quad_perm:[1,0,3,2] row_mask:0xf bank_mask:0xf
	v_add_f32_dpp v56, v56, v56 quad_perm:[1,0,3,2] row_mask:0xf bank_mask:0xf
	v_add_f32_dpp v57, v57, v57 quad_perm:[1,0,3,2] row_mask:0xf bank_mask:0xf
	v_add_f32_dpp v55, v55, v55 quad_perm:[2,3,0,1] row_mask:0xf bank_mask:0xf
	v_add_f32_dpp v56, v56, v56 quad_perm:[2,3,0,1] row_mask:0xf bank_mask:0xf
	v_add_f32_dpp v57, v57, v57 quad_perm:[2,3,0,1] row_mask:0xf bank_mask:0xf
	v_sub_f32_e32 v60, v56, v55
	v_mul_f32_e32 v58, v57, v57
	v_cmp_gt_f32_e32 vcc, 0, v60
	v_mul_f32_e32 v59, v60, v60
	v_fmac_f32_e32 v59, 4.0, v58
	v_sqrt_f32_e32 v59, v59
	v_mul_f32_e32 v63, v62, v41
	v_mul_f32_e32 v43, v62, v40
	v_fma_f32 v40, v61, v40, -v63
	v_fma_f32 v41, v61, v41, v43
	v_add_f32_e64 v59, |v60|, v59
	v_add_f32_e32 v59, 0x0da24260, v59
	v_rcp_f32_e32 v59, v59
	v_add_f32_e32 v58, v57, v57
	v_mul_f32_e32 v59, v58, v59
	v_cndmask_b32_e64 v59, v59, -v59, vcc
	v_fma_f32 v58, v59, v59, 1.0
	v_rsq_f32_e32 v61, v58
	s_nop 0
	v_mul_f32_e32 v62, v61, v59
	v_mul_f32_e32 v55, v62, v54
	v_mul_f32_e32 v56, v62, v52
	v_fma_f32 v52, v61, v52, -v55
	v_fma_f32 v54, v61, v54, v56
	v_mul_f32_e32 v55, v53, v53
	v_mul_f32_e32 v56, v54, v54
	v_mul_f32_e32 v57, v53, v54
	v_add_f32_dpp v55, v55, v55 quad_perm:[1,0,3,2] row_mask:0xf bank_mask:0xf
	v_add_f32_dpp v56, v56, v56 quad_perm:[1,0,3,2] row_mask:0xf bank_mask:0xf
	v_add_f32_dpp v57, v57, v57 quad_perm:[1,0,3,2] row_mask:0xf bank_mask:0xf
	v_add_f32_dpp v55, v55, v55 quad_perm:[2,3,0,1] row_mask:0xf bank_mask:0xf
	v_add_f32_dpp v56, v56, v56 quad_perm:[2,3,0,1] row_mask:0xf bank_mask:0xf
	v_add_f32_dpp v57, v57, v57 quad_perm:[2,3,0,1] row_mask:0xf bank_mask:0xf
	v_sub_f32_e32 v60, v56, v55
	v_mul_f32_e32 v58, v57, v57
	v_cmp_gt_f32_e32 vcc, 0, v60
	v_mul_f32_e32 v59, v60, v60
	v_fmac_f32_e32 v59, 4.0, v58
	v_sqrt_f32_e32 v59, v59
	v_mul_f32_e32 v63, v62, v42
	v_mul_f32_e32 v43, v62, v40
	v_fma_f32 v40, v61, v40, -v63
	v_fma_f32 v42, v61, v42, v43
	v_add_f32_e64 v59, |v60|, v59
	v_add_f32_e32 v59, 0x0da24260, v59
	v_rcp_f32_e32 v59, v59
	v_add_f32_e32 v58, v57, v57
	v_mul_f32_e32 v59, v58, v59
	v_cndmask_b32_e64 v59, v59, -v59, vcc
	v_fma_f32 v58, v59, v59, 1.0
	v_rsq_f32_e32 v61, v58
	s_nop 0
	v_mul_f32_e32 v62, v61, v59
	v_mul_f32_e32 v55, v62, v54
	v_mul_f32_e32 v56, v62, v53
	v_fma_f32 v53, v61, v53, -v55
	v_fma_f32 v54, v61, v54, v56
	v_mul_f32_e32 v55, v52, v52
	v_mul_f32_e32 v56, v53, v53
	v_mul_f32_e32 v57, v52, v53
	v_add_f32_dpp v55, v55, v55 quad_perm:[1,0,3,2] row_mask:0xf bank_mask:0xf
	v_add_f32_dpp v56, v56, v56 quad_perm:[1,0,3,2] row_mask:0xf bank_mask:0xf
	v_add_f32_dpp v57, v57, v57 quad_perm:[1,0,3,2] row_mask:0xf bank_mask:0xf
	v_add_f32_dpp v55, v55, v55 quad_perm:[2,3,0,1] row_mask:0xf bank_mask:0xf
	v_add_f32_dpp v56, v56, v56 quad_perm:[2,3,0,1] row_mask:0xf bank_mask:0xf
	v_add_f32_dpp v57, v57, v57 quad_perm:[2,3,0,1] row_mask:0xf bank_mask:0xf
	v_sub_f32_e32 v60, v56, v55
	v_mul_f32_e32 v58, v57, v57
	v_cmp_gt_f32_e32 vcc, 0, v60
	v_mul_f32_e32 v59, v60, v60
	v_fmac_f32_e32 v59, 4.0, v58
	v_sqrt_f32_e32 v59, v59
	v_mul_f32_e32 v63, v62, v42
	v_mul_f32_e32 v43, v62, v41
	v_fma_f32 v41, v61, v41, -v63
	v_fma_f32 v42, v61, v42, v43
	v_add_f32_e64 v59, |v60|, v59
	v_add_f32_e32 v59, 0x0da24260, v59
	v_rcp_f32_e32 v59, v59
	v_add_f32_e32 v58, v57, v57
	v_mul_f32_e32 v59, v58, v59
	v_cndmask_b32_e64 v59, v59, -v59, vcc
	v_fma_f32 v58, v59, v59, 1.0
	v_rsq_f32_e32 v61, v58
	s_nop 0
	v_mul_f32_e32 v62, v61, v59
	v_mul_f32_e32 v55, v62, v53
	v_mul_f32_e32 v56, v62, v52
	v_fma_f32 v52, v61, v52, -v55
	v_fma_f32 v53, v61, v53, v56
	v_mul_f32_e32 v55, v52, v52
	v_mul_f32_e32 v56, v54, v54
	v_mul_f32_e32 v57, v52, v54
	v_add_f32_dpp v55, v55, v55 quad_perm:[1,0,3,2] row_mask:0xf bank_mask:0xf
	v_add_f32_dpp v56, v56, v56 quad_perm:[1,0,3,2] row_mask:0xf bank_mask:0xf
	v_add_f32_dpp v57, v57, v57 quad_perm:[1,0,3,2] row_mask:0xf bank_mask:0xf
	v_add_f32_dpp v55, v55, v55 quad_perm:[2,3,0,1] row_mask:0xf bank_mask:0xf
	v_add_f32_dpp v56, v56, v56 quad_perm:[2,3,0,1] row_mask:0xf bank_mask:0xf
	v_add_f32_dpp v57, v57, v57 quad_perm:[2,3,0,1] row_mask:0xf bank_mask:0xf
	v_sub_f32_e32 v60, v56, v55
	v_mul_f32_e32 v58, v57, v57
	v_cmp_gt_f32_e32 vcc, 0, v60
	v_mul_f32_e32 v59, v60, v60
	v_fmac_f32_e32 v59, 4.0, v58
	v_sqrt_f32_e32 v59, v59
	v_mul_f32_e32 v63, v62, v41
	v_mul_f32_e32 v43, v62, v40
	v_fma_f32 v40, v61, v40, -v63
	v_fma_f32 v41, v61, v41, v43
	v_add_f32_e64 v59, |v60|, v59
	v_add_f32_e32 v59, 0x0da24260, v59
	v_rcp_f32_e32 v59, v59
	v_add_f32_e32 v58, v57, v57
	v_mul_f32_e32 v59, v58, v59
	v_cndmask_b32_e64 v59, v59, -v59, vcc
	v_fma_f32 v58, v59, v59, 1.0
	v_rsq_f32_e32 v61, v58
	s_nop 0
	v_mul_f32_e32 v62, v61, v59
	v_mul_f32_e32 v55, v62, v54
	v_mul_f32_e32 v56, v62, v52
	v_fma_f32 v52, v61, v52, -v55
	v_fma_f32 v54, v61, v54, v56
	v_mul_f32_e32 v55, v53, v53
	v_mul_f32_e32 v56, v54, v54
	v_mul_f32_e32 v57, v53, v54
	v_add_f32_dpp v55, v55, v55 quad_perm:[1,0,3,2] row_mask:0xf bank_mask:0xf
	v_add_f32_dpp v56, v56, v56 quad_perm:[1,0,3,2] row_mask:0xf bank_mask:0xf
	v_add_f32_dpp v57, v57, v57 quad_perm:[1,0,3,2] row_mask:0xf bank_mask:0xf
	v_add_f32_dpp v55, v55, v55 quad_perm:[2,3,0,1] row_mask:0xf bank_mask:0xf
	v_add_f32_dpp v56, v56, v56 quad_perm:[2,3,0,1] row_mask:0xf bank_mask:0xf
	v_add_f32_dpp v57, v57, v57 quad_perm:[2,3,0,1] row_mask:0xf bank_mask:0xf
	v_sub_f32_e32 v60, v56, v55
	v_mul_f32_e32 v58, v57, v57
	v_cmp_gt_f32_e32 vcc, 0, v60
	v_mul_f32_e32 v59, v60, v60
	v_fmac_f32_e32 v59, 4.0, v58
	v_sqrt_f32_e32 v59, v59
	v_mul_f32_e32 v63, v62, v42
	v_mul_f32_e32 v43, v62, v40
	v_fma_f32 v40, v61, v40, -v63
	v_fma_f32 v42, v61, v42, v43
	v_add_f32_e64 v59, |v60|, v59
	v_add_f32_e32 v59, 0x0da24260, v59
	v_rcp_f32_e32 v59, v59
	v_add_f32_e32 v58, v57, v57
	v_mul_f32_e32 v59, v58, v59
	v_cndmask_b32_e64 v59, v59, -v59, vcc
	v_fma_f32 v58, v59, v59, 1.0
	v_rsq_f32_e32 v61, v58
	s_nop 0
	v_mul_f32_e32 v62, v61, v59
	v_mul_f32_e32 v55, v62, v54
	v_mul_f32_e32 v56, v62, v53
	v_fma_f32 v53, v61, v53, -v55
	v_fma_f32 v54, v61, v54, v56
	v_mul_f32_e32 v55, v52, v52
	v_mul_f32_e32 v56, v53, v53
	v_mul_f32_e32 v57, v52, v53
	v_add_f32_dpp v55, v55, v55 quad_perm:[1,0,3,2] row_mask:0xf bank_mask:0xf
	v_add_f32_dpp v56, v56, v56 quad_perm:[1,0,3,2] row_mask:0xf bank_mask:0xf
	v_add_f32_dpp v57, v57, v57 quad_perm:[1,0,3,2] row_mask:0xf bank_mask:0xf
	v_add_f32_dpp v55, v55, v55 quad_perm:[2,3,0,1] row_mask:0xf bank_mask:0xf
	v_add_f32_dpp v56, v56, v56 quad_perm:[2,3,0,1] row_mask:0xf bank_mask:0xf
	v_add_f32_dpp v57, v57, v57 quad_perm:[2,3,0,1] row_mask:0xf bank_mask:0xf
	v_sub_f32_e32 v60, v56, v55
	v_mul_f32_e32 v58, v57, v57
	v_cmp_gt_f32_e32 vcc, 0, v60
	v_mul_f32_e32 v59, v60, v60
	v_fmac_f32_e32 v59, 4.0, v58
	v_sqrt_f32_e32 v59, v59
	v_mul_f32_e32 v63, v62, v42
	v_mul_f32_e32 v43, v62, v41
	v_fma_f32 v41, v61, v41, -v63
	v_fma_f32 v42, v61, v42, v43
	v_add_f32_e64 v59, |v60|, v59
	v_add_f32_e32 v59, 0x0da24260, v59
	v_rcp_f32_e32 v59, v59
	v_add_f32_e32 v58, v57, v57
	v_mul_f32_e32 v59, v58, v59
	v_cndmask_b32_e64 v59, v59, -v59, vcc
	v_fma_f32 v58, v59, v59, 1.0
	v_rsq_f32_e32 v61, v58
	s_nop 0
	v_mul_f32_e32 v62, v61, v59
	v_mul_f32_e32 v55, v62, v53
	v_mul_f32_e32 v56, v62, v52
	v_fma_f32 v52, v61, v52, -v55
	v_fma_f32 v53, v61, v53, v56
	v_mul_f32_e32 v55, v52, v52
	v_mul_f32_e32 v56, v54, v54
	v_mul_f32_e32 v57, v52, v54
	v_add_f32_dpp v55, v55, v55 quad_perm:[1,0,3,2] row_mask:0xf bank_mask:0xf
	v_add_f32_dpp v56, v56, v56 quad_perm:[1,0,3,2] row_mask:0xf bank_mask:0xf
	v_add_f32_dpp v57, v57, v57 quad_perm:[1,0,3,2] row_mask:0xf bank_mask:0xf
	v_add_f32_dpp v55, v55, v55 quad_perm:[2,3,0,1] row_mask:0xf bank_mask:0xf
	v_add_f32_dpp v56, v56, v56 quad_perm:[2,3,0,1] row_mask:0xf bank_mask:0xf
	v_add_f32_dpp v57, v57, v57 quad_perm:[2,3,0,1] row_mask:0xf bank_mask:0xf
	v_sub_f32_e32 v60, v56, v55
	v_mul_f32_e32 v58, v57, v57
	v_cmp_gt_f32_e32 vcc, 0, v60
	v_mul_f32_e32 v59, v60, v60
	v_fmac_f32_e32 v59, 4.0, v58
	v_sqrt_f32_e32 v59, v59
	v_mul_f32_e32 v63, v62, v41
	v_mul_f32_e32 v43, v62, v40
	v_fma_f32 v40, v61, v40, -v63
	v_fma_f32 v41, v61, v41, v43
	v_add_f32_e64 v59, |v60|, v59
	v_add_f32_e32 v59, 0x0da24260, v59
	v_rcp_f32_e32 v59, v59
	v_add_f32_e32 v58, v57, v57
	v_mul_f32_e32 v59, v58, v59
	v_cndmask_b32_e64 v59, v59, -v59, vcc
	v_fma_f32 v58, v59, v59, 1.0
	v_rsq_f32_e32 v61, v58
	s_nop 0
	v_mul_f32_e32 v62, v61, v59
	v_mul_f32_e32 v55, v62, v54
	v_mul_f32_e32 v56, v62, v52
	v_fma_f32 v52, v61, v52, -v55
	v_fma_f32 v54, v61, v54, v56
	v_mul_f32_e32 v55, v53, v53
	v_mul_f32_e32 v56, v54, v54
	v_mul_f32_e32 v57, v53, v54
	v_add_f32_dpp v55, v55, v55 quad_perm:[1,0,3,2] row_mask:0xf bank_mask:0xf
	v_add_f32_dpp v56, v56, v56 quad_perm:[1,0,3,2] row_mask:0xf bank_mask:0xf
	v_add_f32_dpp v57, v57, v57 quad_perm:[1,0,3,2] row_mask:0xf bank_mask:0xf
	v_add_f32_dpp v55, v55, v55 quad_perm:[2,3,0,1] row_mask:0xf bank_mask:0xf
	v_add_f32_dpp v56, v56, v56 quad_perm:[2,3,0,1] row_mask:0xf bank_mask:0xf
	v_add_f32_dpp v57, v57, v57 quad_perm:[2,3,0,1] row_mask:0xf bank_mask:0xf
	v_sub_f32_e32 v60, v56, v55
	v_mul_f32_e32 v58, v57, v57
	v_cmp_gt_f32_e32 vcc, 0, v60
	v_mul_f32_e32 v59, v60, v60
	v_fmac_f32_e32 v59, 4.0, v58
	v_sqrt_f32_e32 v59, v59
	v_mul_f32_e32 v63, v62, v42
	v_mul_f32_e32 v43, v62, v40
	v_fma_f32 v40, v61, v40, -v63
	v_fma_f32 v42, v61, v42, v43
	v_add_f32_e64 v59, |v60|, v59
	v_add_f32_e32 v59, 0x0da24260, v59
	v_rcp_f32_e32 v59, v59
	v_add_f32_e32 v58, v57, v57
	v_mul_f32_e32 v59, v58, v59
	v_cndmask_b32_e64 v59, v59, -v59, vcc
	v_fma_f32 v58, v59, v59, 1.0
	v_rsq_f32_e32 v61, v58
	s_nop 0
	v_mul_f32_e32 v62, v61, v59
	v_mul_f32_e32 v55, v62, v54
	v_mul_f32_e32 v56, v62, v53
	v_fma_f32 v53, v61, v53, -v55
	v_fma_f32 v54, v61, v54, v56
	v_mul_f32_e32 v63, v62, v42
	v_mul_f32_e32 v43, v62, v41
	v_fma_f32 v41, v61, v41, -v63
	v_fma_f32 v42, v61, v42, v43
	v_mul_f32_e32 v55, v52, v52
	v_mul_f32_e32 v56, v53, v53
	v_mul_f32_e32 v57, v54, v54
	v_add_f32_dpp v55, v55, v55 quad_perm:[1,0,3,2] row_mask:0xf bank_mask:0xf
	v_add_f32_dpp v56, v56, v56 quad_perm:[1,0,3,2] row_mask:0xf bank_mask:0xf
	v_add_f32_dpp v57, v57, v57 quad_perm:[1,0,3,2] row_mask:0xf bank_mask:0xf
	v_add_f32_dpp v55, v55, v55 quad_perm:[2,3,0,1] row_mask:0xf bank_mask:0xf
	v_add_f32_dpp v56, v56, v56 quad_perm:[2,3,0,1] row_mask:0xf bank_mask:0xf
	v_add_f32_dpp v57, v57, v57 quad_perm:[2,3,0,1] row_mask:0xf bank_mask:0xf
	v_cmp_le_f32_e64 s[28:29], v55, v56
	v_cmp_le_f32_e64 s[30:31], v55, v57
	v_cmp_lt_f32_e32 vcc, v57, v56
	s_and_b64 s[28:29], s[28:29], s[30:31]
	s_andn2_b64 s[30:31], vcc, s[28:29]
	v_cndmask_b32_e64 v44, v52, v53, s[28:29]
	v_cndmask_b32_e64 v45, v54, v53, s[30:31]
	v_cndmask_b32_e64 v46, v40, v41, s[28:29]
	v_cndmask_b32_e64 v47, v42, v41, s[30:31]
	v_mul_f32_e32 v58, v44, v44
	s_nop 1
	v_add_f32_dpp v58, v58, v58 quad_perm:[1,0,3,2] row_mask:0xf bank_mask:0xf
	s_nop 1
	v_add_f32_dpp v58, v58, v58 quad_perm:[2,3,0,1] row_mask:0xf bank_mask:0xf
	v_max_f32_e32 v58, 0x3aa2425, v58
	v_rsq_f32_e32 v58, v58
	s_nop 0
	v_mul_f32_e32 v48, v44, v58
	v_mul_f32_e32 v59, v48, v45
	s_nop 1
	v_add_f32_dpp v59, v59, v59 quad_perm:[1,0,3,2] row_mask:0xf bank_mask:0xf
	s_nop 1
	v_add_f32_dpp v59, v59, v59 quad_perm:[2,3,0,1] row_mask:0xf bank_mask:0xf
	v_fma_f32 v49, -v59, v48, v45
	v_mul_f32_e32 v58, v49, v49
	s_nop 1
	v_add_f32_dpp v58, v58, v58 quad_perm:[1,0,3,2] row_mask:0xf bank_mask:0xf
	s_nop 1
	v_add_f32_dpp v58, v58, v58 quad_perm:[2,3,0,1] row_mask:0xf bank_mask:0xf
	v_max_f32_e32 v58, 0x3aa2425, v58
	v_rsq_f32_e32 v58, v58
	s_nop 0
	v_mul_f32_e32 v50, v49, v58
	v_mov_b32_dpp v43, v47 quad_perm:[2,0,1,3] row_mask:0xf bank_mask:0xf
	v_mov_b32_dpp v63, v47 quad_perm:[1,2,0,3] row_mask:0xf bank_mask:0xf
	v_mov_b32_dpp v62, v50 quad_perm:[2,0,1,3] row_mask:0xf bank_mask:0xf
	v_mov_b32_dpp v61, v50 quad_perm:[1,2,0,3] row_mask:0xf bank_mask:0xf
	v_mul_f32_dpp v60, v46, v43 quad_perm:[1,2,0,3] row_mask:0xf bank_mask:0xf
	v_mul_f32_dpp v51, v48, v62 quad_perm:[1,2,0,3] row_mask:0xf bank_mask:0xf
	s_nop 0
	v_fmac_f32_dpp v60, -v46, v63 quad_perm:[2,0,1,3] row_mask:0xf bank_mask:0xf
	v_fmac_f32_dpp v51, -v48, v61 quad_perm:[2,0,1,3] row_mask:0xf bank_mask:0xf
	v_mul_f32_dpp v52, v46, v48 quad_perm:[0,0,0,0] row_mask:0xf bank_mask:0xf
	v_mul_f32_dpp v53, v46, v48 quad_perm:[1,1,1,1] row_mask:0xf bank_mask:0xf
	v_mul_f32_dpp v54, v46, v48 quad_perm:[2,2,2,2] row_mask:0xf bank_mask:0xf
	v_fmac_f32_dpp v52, v47, v50 quad_perm:[0,0,0,0] row_mask:0xf bank_mask:0xf
	v_fmac_f32_dpp v53, v47, v50 quad_perm:[1,1,1,1] row_mask:0xf bank_mask:0xf
	v_fmac_f32_dpp v54, v47, v50 quad_perm:[2,2,2,2] row_mask:0xf bank_mask:0xf
	v_fmac_f32_dpp v52, v60, v51 quad_perm:[0,0,0,0] row_mask:0xf bank_mask:0xf
	v_fmac_f32_dpp v53, v60, v51 quad_perm:[1,1,1,1] row_mask:0xf bank_mask:0xf
	v_fmac_f32_dpp v54, v60, v51 quad_perm:[2,2,2,2] row_mask:0xf bank_mask:0xf
	v_mov_b32_e32 v55, 0
	v_writelane_b32 v55, s32, 48
	v_writelane_b32 v55, s33, 49
	v_writelane_b32 v55, s34, 50
	v_mul_f32_e32 v55, 0xbc800000, v55
	v_mul_f32_e32 v56, v55, v52
	v_mul_f32_e32 v57, v55, v53
	v_mul_f32_e32 v58, v55, v54
	v_add_f32_dpp v56, v56, v56 quad_perm:[1,0,3,2] row_mask:0xf bank_mask:0xf
	v_add_f32_dpp v57, v57, v57 quad_perm:[1,0,3,2] row_mask:0xf bank_mask:0xf
	v_add_f32_dpp v58, v58, v58 quad_perm:[1,0,3,2] row_mask:0xf bank_mask:0xf
	v_add_f32_dpp v56, v56, v56 quad_perm:[2,3,0,1] row_mask:0xf bank_mask:0xf
	v_add_f32_dpp v57, v57, v57 quad_perm:[2,3,0,1] row_mask:0xf bank_mask:0xf
	v_add_f32_dpp v58, v58, v58 quad_perm:[2,3,0,1] row_mask:0xf bank_mask:0xf
	v_cndmask_b32_e64 v52, v52, v56, s[26:27]
	v_cndmask_b32_e64 v53, v53, v57, s[26:27]
	v_cndmask_b32_e64 v54, v54, v58, s[26:27]
	v_subrev_u32_e32 v59, 48, v0
	v_lshlrev_b32_e32 v59, 4, v59
	s_mov_b32 s20, 0
	s_mov_b32 s21, 0xf0000
	s_mov_b64 exec, s[20:21]
	ds_write_b96 v59, v[52:54] offset:24576
	s_mov_b64 exec, -1
	s_waitcnt lgkmcnt(0)
	s_branch .Ljoin
